# k10 plus GLA output / chunk-summary units: q,k,v,S_prev loads issued behind the first batch (one round trip per unit instead of three)
# speedup vs baseline: 1.0123x; 1.0001x over previous
.LBB0_641:
	s_ashr_i32 s22, s24, 7
	s_and_b32 s26, s24, 31
	s_ashr_i32 s23, s22, 31
	s_lshl_b64 s[10:11], s[22:23], 11
	s_lshl_b32 s12, s26, 6
	s_or_b32 s10, s10, s12
	v_lshl_add_u64 v[36:37], s[10:11], 0, v[24:25]
	v_mov_b64_e32 v[0:1], s[14:15]
	s_bfe_u32 s27, s24, 0x20005
	v_mad_u64_u32 v[0:1], s[10:11], v36, s48, v[0:1]
	v_mad_i32_i24 v1, v37, s48, v1
	s_lshl_b32 s50, s27, 8
	v_lshl_add_u64 v[0:1], v[0:1], 0, s[50:51]
	v_lshl_add_u64 v[0:1], v[0:1], 0, v[208:209]
	s_mov_b64 s[10:11], 0x3d902800
	v_lshl_add_u64 v[2:3], v[0:1], 0, s[10:11]
	s_mov_b32 s10, 0x3d902000
	s_lshl_b32 s50, s27, 9
	v_add_co_u32_e64 v0, s[10:11], s10, v0
	v_lshl_add_u64 v[20:21], v[26:27], 0, s[50:51]
	s_nop 0
	v_addc_co_u32_e64 v1, s[10:11], 0, v1, s[10:11]
	global_load_dwordx4 v[12:15], v[0:1], off offset:2048
	s_nop 0
	global_load_dwordx4 v[0:3], v[2:3], off offset:16
	s_nop 0
	global_load_dwordx4 v[4:7], v[20:21], off offset:48
	global_load_dwordx4 v[8:11], v[20:21], off offset:32
	global_load_dwordx4 v[16:19], v[20:21], off offset:16
	s_nop 0
	global_load_dwordx4 v[20:23], v[20:21], off
	v_mad_u64_u32 v[152:153], s[12:13], v36, s48, 0
	v_mad_i32_i24 v153, v37, s48, v153
	v_lshl_add_u64 v[152:153], s[16:17], 0, v[152:153]
	v_mov_b32_e32 v154, s27
	v_lshlrev_b32_e32 v154, 8, v154
	v_mov_b32_e32 v155, v209
	v_lshl_add_u64 v[156:157], v[152:153], 0, v[154:155]
	v_mov_b32_e32 v158, v32
	v_mov_b32_e32 v159, v209
	v_lshl_add_u64 v[156:157], v[156:157], 0, v[158:159]
	s_mov_b64 s[12:13], 0x1400
	v_lshl_add_u64 v[156:157], v[156:157], 0, s[12:13]
	global_load_dwordx4 v[128:131], v[156:157], off
	global_load_dwordx4 v[132:135], v[156:157], off offset:16
	v_lshl_add_u64 v[160:161], v[152:153], 0, s[50:51]
	v_mov_b32_e32 v158, v34
	v_lshl_add_u64 v[160:161], v[160:161], 0, v[158:159]
	s_mov_b64 s[12:13], 0x1800
	v_lshl_add_u64 v[160:161], v[160:161], 0, s[12:13]
	global_load_dwordx4 v[136:139], v[160:161], off
	global_load_dwordx4 v[140:143], v[160:161], off offset:16
	global_load_dwordx4 v[144:147], v[160:161], off offset:32
	global_load_dwordx4 v[148:151], v[160:161], off offset:48
	s_waitcnt vmcnt(6)
	v_lshlrev_b32_e32 v33, 16, v12
	v_and_b32_e32 v12, 0xffff0000, v12
	v_add_f32_e32 v33, v20, v33
	v_min_f32_e32 v20, 0, v33
	v_mul_f32_e64 v33, |v33|, s89
	v_exp_f32_e32 v33, v33
	v_add_f32_e32 v12, v21, v12
	v_min_f32_e32 v21, 0, v12
	v_mul_f32_e64 v12, |v12|, s89
	v_add_f32_e32 v33, 1.0, v33
	v_cmp_gt_f32_e64 s[10:11], s33, v33
	v_exp_f32_e32 v12, v12
	s_nop 0
	v_cndmask_b32_e64 v35, 0, 32, s[10:11]
	v_ldexp_f32 v33, v33, v35
	v_log_f32_e32 v33, v33
	v_add_f32_e32 v12, 1.0, v12
	v_mul_f32_e32 v35, 0x3f317217, v33
	v_fma_f32 v35, v33, s83, -v35
	v_fmac_f32_e32 v35, 0x3377d1cf, v33
	v_fmac_f32_e32 v35, 0x3f317217, v33
	v_cmp_lt_f32_e64 s[12:13], |v33|, s93
	s_nop 1
	v_cndmask_b32_e64 v33, v33, v35, s[12:13]
	v_cndmask_b32_e64 v35, 0, v241, s[10:11]
	v_cmp_gt_f32_e64 s[10:11], s33, v12
	v_sub_f32_e32 v52, v33, v35
	s_nop 0
	v_cndmask_b32_e64 v33, 0, 32, s[10:11]
	v_ldexp_f32 v12, v12, v33
	v_log_f32_e32 v12, v12
	s_nop 0
	v_mul_f32_e32 v33, 0x3f317217, v12
	v_fma_f32 v33, v12, s83, -v33
	v_fmac_f32_e32 v33, 0x3377d1cf, v12
	v_fmac_f32_e32 v33, 0x3f317217, v12
	v_cmp_lt_f32_e64 s[12:13], |v12|, s93
	s_nop 1
	v_cndmask_b32_e64 v12, v12, v33, s[12:13]
	v_cndmask_b32_e64 v33, 0, v241, s[10:11]
	v_sub_f32_e32 v53, v12, v33
	v_lshlrev_b32_e32 v12, 16, v13
	v_add_f32_e32 v22, v22, v12
	v_min_f32_e32 v12, 0, v22
	v_mul_f32_e64 v22, |v22|, s89
	v_exp_f32_e32 v22, v22
	v_and_b32_e32 v13, 0xffff0000, v13
	v_add_f32_e32 v23, v23, v13
	v_min_f32_e32 v13, 0, v23
	v_add_f32_e32 v22, 1.0, v22
	v_cmp_gt_f32_e64 s[10:11], s33, v22
	v_mul_f32_e64 v23, |v23|, s89
	v_exp_f32_e32 v23, v23
	v_cndmask_b32_e64 v33, 0, 32, s[10:11]
	v_ldexp_f32 v22, v22, v33
	v_log_f32_e32 v22, v22
	v_add_f32_e32 v23, 1.0, v23
	v_pk_add_f32 v[20:21], v[20:21], v[52:53] neg_lo:[0,1] neg_hi:[0,1]
	v_mul_f32_e32 v33, 0x3f317217, v22
	v_fma_f32 v33, v22, s83, -v33
	v_fmac_f32_e32 v33, 0x3377d1cf, v22
	v_fmac_f32_e32 v33, 0x3f317217, v22
	v_cmp_lt_f32_e64 s[12:13], |v22|, s93
	v_pk_mul_f32 v[20:21], v[20:21], s[76:77] op_sel_hi:[1,0]
	s_nop 0
	v_cndmask_b32_e64 v22, v22, v33, s[12:13]
	v_cndmask_b32_e64 v33, 0, v241, s[10:11]
	v_cmp_gt_f32_e64 s[10:11], s33, v23
	v_sub_f32_e32 v22, v22, v33
	s_nop 0
	v_cndmask_b32_e64 v33, 0, 32, s[10:11]
	v_ldexp_f32 v23, v23, v33
	v_log_f32_e32 v23, v23
	s_nop 0
	v_mul_f32_e32 v33, 0x3f317217, v23
	v_fma_f32 v33, v23, s83, -v33
	v_fmac_f32_e32 v33, 0x3377d1cf, v23
	v_fmac_f32_e32 v33, 0x3f317217, v23
	v_cmp_lt_f32_e64 s[12:13], |v23|, s93
	s_nop 1
	v_cndmask_b32_e64 v23, v23, v33, s[12:13]
	v_cndmask_b32_e64 v33, 0, v241, s[10:11]
	v_sub_f32_e32 v23, v23, v33
	v_pk_add_f32 v[12:13], v[12:13], v[22:23] neg_lo:[0,1] neg_hi:[0,1]
	v_mov_b32_e32 v33, 0
	v_pk_mul_f32 v[22:23], v[12:13], s[76:77] op_sel_hi:[1,0]
	v_lshlrev_b32_e32 v12, 16, v14
	v_add_f32_e32 v13, v16, v12
	v_min_f32_e32 v12, 0, v13
	v_mul_f32_e64 v13, |v13|, s89
	v_exp_f32_e32 v13, v13
	ds_write_b128 v38, v[20:23]
	v_add_u32_e32 v20, 0x1c00, v50
	v_add_f32_e32 v13, 1.0, v13
	v_cmp_gt_f32_e64 s[10:11], s33, v13
	s_nop 1
	v_cndmask_b32_e64 v16, 0, 32, s[10:11]
	v_ldexp_f32 v13, v13, v16
	v_log_f32_e32 v13, v13
	s_nop 0
	v_mul_f32_e32 v16, 0x3f317217, v13
	v_fma_f32 v16, v13, s83, -v16
	v_fmac_f32_e32 v16, 0x3377d1cf, v13
	v_fmac_f32_e32 v16, 0x3f317217, v13
	v_cmp_lt_f32_e64 s[12:13], |v13|, s93
	s_nop 1
	v_cndmask_b32_e64 v13, v13, v16, s[12:13]
	v_cndmask_b32_e64 v16, 0, v241, s[10:11]
	v_sub_f32_e32 v16, v13, v16
	v_and_b32_e32 v13, 0xffff0000, v14
	v_add_f32_e32 v14, v17, v13
	v_min_f32_e32 v13, 0, v14
	v_mul_f32_e64 v14, |v14|, s89
	v_exp_f32_e32 v14, v14
	s_nop 0
	v_add_f32_e32 v14, 1.0, v14
	v_cmp_gt_f32_e64 s[10:11], s33, v14
	s_nop 1
	v_cndmask_b32_e64 v17, 0, 32, s[10:11]
	v_ldexp_f32 v14, v14, v17
	v_log_f32_e32 v14, v14
	s_nop 0
	v_mul_f32_e32 v17, 0x3f317217, v14
	v_fma_f32 v17, v14, s83, -v17
	v_fmac_f32_e32 v17, 0x3377d1cf, v14
	v_fmac_f32_e32 v17, 0x3f317217, v14
	v_cmp_lt_f32_e64 s[12:13], |v14|, s93
	s_nop 1
	v_cndmask_b32_e64 v14, v14, v17, s[12:13]
	v_cndmask_b32_e64 v17, 0, v241, s[10:11]
	v_sub_f32_e32 v17, v14, v17
	v_lshlrev_b32_e32 v14, 16, v15
	v_pk_add_f32 v[12:13], v[12:13], v[16:17] neg_lo:[0,1] neg_hi:[0,1]
	v_add_f32_e32 v16, v18, v14
	v_min_f32_e32 v14, 0, v16
	v_mul_f32_e64 v16, |v16|, s89
	v_exp_f32_e32 v16, v16
	v_and_b32_e32 v15, 0xffff0000, v15
	v_pk_mul_f32 v[12:13], v[12:13], s[76:77] op_sel_hi:[1,0]
	v_add_f32_e32 v16, 1.0, v16
	v_cmp_gt_f32_e64 s[10:11], s33, v16
	s_nop 1
	v_cndmask_b32_e64 v17, 0, 32, s[10:11]
	v_ldexp_f32 v16, v16, v17
	v_log_f32_e32 v16, v16
	s_nop 0
	v_mul_f32_e32 v17, 0x3f317217, v16
	v_fma_f32 v17, v16, s83, -v17
	v_fmac_f32_e32 v17, 0x3377d1cf, v16
	v_fmac_f32_e32 v17, 0x3f317217, v16
	v_cmp_lt_f32_e64 s[12:13], |v16|, s93
	s_nop 1
	v_cndmask_b32_e64 v16, v16, v17, s[12:13]
	v_cndmask_b32_e64 v17, 0, v241, s[10:11]
	v_sub_f32_e32 v16, v16, v17
	v_add_f32_e32 v17, v19, v15
	v_min_f32_e32 v15, 0, v17
	v_mul_f32_e64 v17, |v17|, s89
	v_exp_f32_e32 v17, v17
	s_nop 0
	v_add_f32_e32 v17, 1.0, v17
	v_cmp_gt_f32_e64 s[10:11], s33, v17
	s_nop 1
	v_cndmask_b32_e64 v18, 0, 32, s[10:11]
	v_ldexp_f32 v17, v17, v18
	v_log_f32_e32 v17, v17
	s_nop 0
	v_mul_f32_e32 v18, 0x3f317217, v17
	v_fma_f32 v18, v17, s83, -v18
	v_fmac_f32_e32 v18, 0x3377d1cf, v17
	v_fmac_f32_e32 v18, 0x3f317217, v17
	v_cmp_lt_f32_e64 s[12:13], |v17|, s93
	s_nop 1
	v_cndmask_b32_e64 v17, v17, v18, s[12:13]
	v_cndmask_b32_e64 v18, 0, v241, s[10:11]
	v_sub_f32_e32 v17, v17, v18
	v_pk_add_f32 v[14:15], v[14:15], v[16:17] neg_lo:[0,1] neg_hi:[0,1]
	s_nop 0
	v_pk_mul_f32 v[14:15], v[14:15], s[76:77] op_sel_hi:[1,0]
	ds_write_b128 v38, v[12:15] offset:16
	v_lshlrev_b32_e32 v12, 16, v0
	v_add_f32_e32 v12, v8, v12
	v_min_f32_e32 v8, 0, v12
	v_mul_f32_e64 v12, |v12|, s89
	v_exp_f32_e32 v12, v12
	v_and_b32_e32 v0, 0xffff0000, v0
	v_add_f32_e32 v0, v9, v0
	v_min_f32_e32 v9, 0, v0
	v_add_f32_e32 v12, 1.0, v12
	v_cmp_gt_f32_e64 s[10:11], s33, v12
	v_mul_f32_e64 v0, |v0|, s89
	v_exp_f32_e32 v0, v0
	v_cndmask_b32_e64 v13, 0, 32, s[10:11]
	v_ldexp_f32 v12, v12, v13
	v_log_f32_e32 v12, v12
	v_add_f32_e32 v0, 1.0, v0
	v_mul_f32_e32 v13, 0x3f317217, v12
	v_fma_f32 v13, v12, s83, -v13
	v_fmac_f32_e32 v13, 0x3377d1cf, v12
	v_fmac_f32_e32 v13, 0x3f317217, v12
	v_cmp_lt_f32_e64 s[12:13], |v12|, s93
	s_nop 1
	v_cndmask_b32_e64 v12, v12, v13, s[12:13]
	v_cndmask_b32_e64 v13, 0, v241, s[10:11]
	v_cmp_gt_f32_e64 s[10:11], s33, v0
	v_sub_f32_e32 v12, v12, v13
	s_nop 0
	v_cndmask_b32_e64 v13, 0, 32, s[10:11]
	v_ldexp_f32 v0, v0, v13
	v_log_f32_e32 v0, v0
	s_nop 0
	v_mul_f32_e32 v13, 0x3f317217, v0
	v_fma_f32 v13, v0, s83, -v13
	v_fmac_f32_e32 v13, 0x3377d1cf, v0
	v_fmac_f32_e32 v13, 0x3f317217, v0
	v_cmp_lt_f32_e64 s[12:13], |v0|, s93
	s_nop 1
	v_cndmask_b32_e64 v0, v0, v13, s[12:13]
	v_cndmask_b32_e64 v13, 0, v241, s[10:11]
	v_sub_f32_e32 v13, v0, v13
	v_lshlrev_b32_e32 v0, 16, v1
	v_add_f32_e32 v10, v10, v0
	v_min_f32_e32 v0, 0, v10
	v_mul_f32_e64 v10, |v10|, s89
	v_exp_f32_e32 v10, v10
	v_pk_add_f32 v[8:9], v[8:9], v[12:13] neg_lo:[0,1] neg_hi:[0,1]
	v_and_b32_e32 v1, 0xffff0000, v1
	v_add_f32_e32 v11, v11, v1
	v_add_f32_e32 v10, 1.0, v10
	v_cmp_gt_f32_e64 s[10:11], s33, v10
	v_min_f32_e32 v1, 0, v11
	v_mul_f32_e64 v11, |v11|, s89
	v_cndmask_b32_e64 v12, 0, 32, s[10:11]
	v_ldexp_f32 v10, v10, v12
	v_log_f32_e32 v10, v10
	v_exp_f32_e32 v11, v11
	v_pk_mul_f32 v[8:9], v[8:9], s[76:77] op_sel_hi:[1,0]
	v_mul_f32_e32 v12, 0x3f317217, v10
	v_fma_f32 v12, v10, s83, -v12
	v_fmac_f32_e32 v12, 0x3377d1cf, v10
	v_fmac_f32_e32 v12, 0x3f317217, v10
	v_cmp_lt_f32_e64 s[12:13], |v10|, s93
	v_add_f32_e32 v11, 1.0, v11
	s_nop 0
	v_cndmask_b32_e64 v10, v10, v12, s[12:13]
	v_cndmask_b32_e64 v12, 0, v241, s[10:11]
	v_cmp_gt_f32_e64 s[10:11], s33, v11
	v_sub_f32_e32 v10, v10, v12
	s_nop 0
	v_cndmask_b32_e64 v12, 0, 32, s[10:11]
	v_ldexp_f32 v11, v11, v12
	v_log_f32_e32 v11, v11
	s_nop 0
	v_mul_f32_e32 v12, 0x3f317217, v11
	v_fma_f32 v12, v11, s83, -v12
	v_fmac_f32_e32 v12, 0x3377d1cf, v11
	v_fmac_f32_e32 v12, 0x3f317217, v11
	v_cmp_lt_f32_e64 s[12:13], |v11|, s93
	s_nop 1
	v_cndmask_b32_e64 v11, v11, v12, s[12:13]
	v_cndmask_b32_e64 v12, 0, v241, s[10:11]
	v_sub_f32_e32 v11, v11, v12
	v_pk_add_f32 v[0:1], v[0:1], v[10:11] neg_lo:[0,1] neg_hi:[0,1]
	v_add_u32_e32 v12, 0x1400, v50
	v_pk_mul_f32 v[10:11], v[0:1], s[76:77] op_sel_hi:[1,0]
	v_lshlrev_b32_e32 v0, 16, v2
	v_add_f32_e32 v1, v4, v0
	v_min_f32_e32 v0, 0, v1
	v_mul_f32_e64 v1, |v1|, s89
	v_exp_f32_e32 v1, v1
	ds_write_b128 v38, v[8:11] offset:32
	v_add_u32_e32 v8, 0xc00, v50
	v_add_f32_e32 v1, 1.0, v1
	v_cmp_gt_f32_e64 s[10:11], s33, v1
	s_nop 1
	v_cndmask_b32_e64 v4, 0, 32, s[10:11]
	v_ldexp_f32 v1, v1, v4
	v_log_f32_e32 v1, v1
	s_nop 0
	v_mul_f32_e32 v4, 0x3f317217, v1
	v_fma_f32 v4, v1, s83, -v4
	v_fmac_f32_e32 v4, 0x3377d1cf, v1
	v_fmac_f32_e32 v4, 0x3f317217, v1
	v_cmp_lt_f32_e64 s[12:13], |v1|, s93
	s_nop 1
	v_cndmask_b32_e64 v1, v1, v4, s[12:13]
	v_cndmask_b32_e64 v4, 0, v241, s[10:11]
	v_sub_f32_e32 v4, v1, v4
	v_and_b32_e32 v1, 0xffff0000, v2
	v_add_f32_e32 v2, v5, v1
	v_min_f32_e32 v1, 0, v2
	v_mul_f32_e64 v2, |v2|, s89
	v_exp_f32_e32 v2, v2
	s_nop 0
	v_add_f32_e32 v2, 1.0, v2
	v_cmp_gt_f32_e64 s[10:11], s33, v2
	s_nop 1
	v_cndmask_b32_e64 v5, 0, 32, s[10:11]
	v_ldexp_f32 v2, v2, v5
	v_log_f32_e32 v2, v2
	s_nop 0
	v_mul_f32_e32 v5, 0x3f317217, v2
	v_fma_f32 v5, v2, s83, -v5
	v_fmac_f32_e32 v5, 0x3377d1cf, v2
	v_fmac_f32_e32 v5, 0x3f317217, v2
	v_cmp_lt_f32_e64 s[12:13], |v2|, s93
	s_nop 1
	v_cndmask_b32_e64 v2, v2, v5, s[12:13]
	v_cndmask_b32_e64 v5, 0, v241, s[10:11]
	v_sub_f32_e32 v5, v2, v5
	v_lshlrev_b32_e32 v2, 16, v3
	v_pk_add_f32 v[0:1], v[0:1], v[4:5] neg_lo:[0,1] neg_hi:[0,1]
	v_add_f32_e32 v4, v6, v2
	v_min_f32_e32 v2, 0, v4
	v_mul_f32_e64 v4, |v4|, s89
	v_exp_f32_e32 v4, v4
	v_and_b32_e32 v3, 0xffff0000, v3
	v_pk_mul_f32 v[0:1], v[0:1], s[76:77] op_sel_hi:[1,0]
	v_add_f32_e32 v4, 1.0, v4
	v_cmp_gt_f32_e64 s[10:11], s33, v4
	s_nop 1
	v_cndmask_b32_e64 v5, 0, 32, s[10:11]
	v_ldexp_f32 v4, v4, v5
	v_log_f32_e32 v4, v4
	s_nop 0
	v_mul_f32_e32 v5, 0x3f317217, v4
	v_fma_f32 v5, v4, s83, -v5
	v_fmac_f32_e32 v5, 0x3377d1cf, v4
	v_fmac_f32_e32 v5, 0x3f317217, v4
	v_cmp_lt_f32_e64 s[12:13], |v4|, s93
	s_nop 1
	v_cndmask_b32_e64 v4, v4, v5, s[12:13]
	v_cndmask_b32_e64 v5, 0, v241, s[10:11]
	v_sub_f32_e32 v4, v4, v5
	v_add_f32_e32 v5, v7, v3
	v_min_f32_e32 v3, 0, v5
	v_mul_f32_e64 v5, |v5|, s89
	v_exp_f32_e32 v5, v5
	s_nop 0
	v_add_f32_e32 v5, 1.0, v5
	v_cmp_gt_f32_e64 s[10:11], s33, v5
	s_nop 1
	v_cndmask_b32_e64 v6, 0, 32, s[10:11]
	v_ldexp_f32 v5, v5, v6
	v_log_f32_e32 v5, v5
	s_nop 0
	v_mul_f32_e32 v6, 0x3f317217, v5
	v_fma_f32 v6, v5, s83, -v6
	v_fmac_f32_e32 v6, 0x3377d1cf, v5
	v_fmac_f32_e32 v6, 0x3f317217, v5
	v_cmp_lt_f32_e64 s[12:13], |v5|, s93
	s_nop 1
	v_cndmask_b32_e64 v5, v5, v6, s[12:13]
	v_cndmask_b32_e64 v6, 0, v241, s[10:11]
	v_sub_f32_e32 v5, v5, v6
	v_pk_add_f32 v[2:3], v[2:3], v[4:5] neg_lo:[0,1] neg_hi:[0,1]
	s_nop 0
	v_pk_mul_f32 v[2:3], v[2:3], s[76:77] op_sel_hi:[1,0]
	ds_write_b128 v38, v[0:3] offset:48
	s_waitcnt lgkmcnt(0)
	s_barrier
	ds_read2_b32 v[0:1], v50 offset1:132
	v_add_u32_e32 v2, 0x400, v50
	ds_read2_b32 v[4:5], v2 offset0:8 offset1:140
	v_add_u32_e32 v3, 0x800, v50
	ds_read2_b32 v[6:7], v3 offset0:16 offset1:148
	s_waitcnt lgkmcnt(2)
	v_add_f32_e32 v0, 0, v0
	v_add_f32_e32 v1, v0, v1
	ds_read2_b32 v[10:11], v8 offset0:24 offset1:156
	s_waitcnt lgkmcnt(2)
	v_add_f32_e32 v4, v1, v4
	v_add_f32_e32 v5, v4, v5
	s_waitcnt lgkmcnt(1)
	v_add_f32_e32 v6, v5, v6
	v_add_f32_e32 v7, v6, v7
	s_waitcnt lgkmcnt(0)
	v_add_f32_e32 v9, v7, v10
	v_add_f32_e32 v10, v9, v11
	v_add_u32_e32 v11, 0x1000, v50
	ds_read2_b32 v[14:15], v11 offset0:32 offset1:164
	ds_read2_b32 v[16:17], v12 offset0:40 offset1:172
	ds_read2_b32 v[22:23], v20 offset0:56 offset1:188
	s_waitcnt lgkmcnt(2)
	v_add_f32_e32 v13, v10, v14
	v_add_f32_e32 v14, v13, v15
	s_waitcnt lgkmcnt(1)
	v_add_f32_e32 v15, v14, v16
	v_add_f32_e32 v16, v15, v17
	v_add_u32_e32 v17, 0x1800, v50
	ds_read2_b32 v[18:19], v17 offset0:48 offset1:180
	s_waitcnt lgkmcnt(0)
	v_add_f32_e32 v18, v16, v18
	v_add_f32_e32 v19, v18, v19
	v_add_f32_e32 v21, v19, v22
	v_add_f32_e32 v22, v21, v23
	v_mov_b32_e32 v23, 0
	ds_write_b32 v39, v22
	s_waitcnt lgkmcnt(0)
	s_barrier
	s_and_saveexec_b64 s[10:11], vcc
	s_cbranch_execz .LBB0_651
	ds_read_b32 v33, v40
	s_waitcnt lgkmcnt(0)
	v_add_f32_e32 v33, 0, v33
	s_or_b64 exec, exec, s[10:11]
	v_mov_b32_e32 v35, 0
	s_and_saveexec_b64 s[10:11], s[2:3]
	s_cbranch_execnz .LBB0_652

.LBB0_645:
	s_or_b64 exec, exec, s[10:11]
	s_waitcnt lgkmcnt(0)
	v_add_f32_e32 v33, v33, v35
	v_add_f32_e32 v23, v33, v23
	v_add_f32_e32 v0, v0, v23
	v_add_f32_e32 v1, v1, v23
	ds_write2_b32 v50, v0, v1 offset1:132
	v_add_f32_e32 v0, v4, v23
	v_add_f32_e32 v1, v5, v23
	ds_write2_b32 v2, v0, v1 offset0:8 offset1:140
	v_add_f32_e32 v0, v6, v23
	v_add_f32_e32 v1, v7, v23
	ds_write2_b32 v3, v0, v1 offset0:16 offset1:148
	v_add_f32_e32 v0, v9, v23
	v_add_f32_e32 v1, v10, v23
	ds_write2_b32 v8, v0, v1 offset0:24 offset1:156
	v_add_f32_e32 v0, v13, v23
	v_add_f32_e32 v1, v14, v23
	ds_write2_b32 v11, v0, v1 offset0:32 offset1:164
	v_add_f32_e32 v0, v15, v23
	v_add_f32_e32 v1, v16, v23
	ds_write2_b32 v12, v0, v1 offset0:40 offset1:172
	v_add_f32_e32 v0, v18, v23
	v_add_f32_e32 v1, v19, v23
	ds_write2_b32 v17, v0, v1 offset0:48 offset1:180
	v_add_f32_e32 v1, v21, v23
	v_add_f32_e32 v0, v22, v23
	ds_write2_b32 v20, v1, v0 offset0:56 offset1:188
	s_and_saveexec_b64 s[10:11], s[6:7]
	ds_write_b32 v41, v0
	s_or_b64 exec, exec, s[10:11]
	v_mad_u64_u32 v[0:1], s[10:11], v36, s48, 0
	v_mad_i32_i24 v1, v37, s48, v1
	s_lshl_b32 s10, s27, 7
	s_lshl_b32 s11, s22, 2
	s_or_b32 s22, s11, s27
	v_lshl_add_u64 v[36:37], s[16:17], 0, v[0:1]
	s_lshl_b32 s10, s10, 1
	s_mov_b32 s11, s51
	v_lshl_add_u64 v[0:1], v[36:37], 0, s[10:11]
	v_mov_b32_e32 v33, v209
	v_lshl_add_u64 v[0:1], v[0:1], 0, v[32:33]
	s_mov_b64 s[10:11], 0x1400
	s_movk_i32 s12, 0x1000
	v_lshl_add_u64 v[4:5], v[0:1], 0, s[10:11]
	v_add_co_u32_e64 v0, s[10:11], s12, v0
	s_waitcnt lgkmcnt(0)
	s_nop 0
	v_addc_co_u32_e64 v1, s[10:11], 0, v1, s[10:11]
	s_barrier
	s_waitcnt vmcnt(0)
	v_mov_b32_e32 v0, v128
	v_mov_b32_e32 v1, v129
	v_mov_b32_e32 v2, v130
	v_mov_b32_e32 v3, v131
	v_mov_b32_e32 v4, v132
	v_mov_b32_e32 v5, v133
	v_mov_b32_e32 v6, v134
	v_mov_b32_e32 v7, v135
	ds_read_b128 v[8:11], v43
	ds_read_b128 v[12:15], v43 offset:16
	ds_read_b128 v[16:19], v42
	ds_read_b128 v[20:23], v42 offset:16
	v_mov_b32_e32 v35, v209
	s_mov_b64 s[10:11], 0x1800
	s_waitcnt lgkmcnt(1)
	v_sub_f32_e32 v8, v8, v16
	v_sub_f32_e32 v9, v9, v17
	v_mul_f32_e32 v8, 0x3fb8aa3b, v8
	v_mul_f32_e32 v9, 0x3fb8aa3b, v9
	v_exp_f32_e32 v8, v8
	v_exp_f32_e32 v9, v9
	s_waitcnt vmcnt(1)
	v_lshlrev_b32_e32 v16, 16, v0
	v_and_b32_e32 v17, 0xffff0000, v0
	v_sub_f32_e32 v0, v10, v18
	v_mul_f32_e32 v0, 0x3fb8aa3b, v0
	v_exp_f32_e32 v10, v0
	v_sub_f32_e32 v0, v11, v19
	v_mul_f32_e32 v0, 0x3fb8aa3b, v0
	v_exp_f32_e32 v11, v0
	v_lshlrev_b32_e32 v0, 16, v1
	v_and_b32_e32 v1, 0xffff0000, v1
	v_pk_mul_f32 v[8:9], v[8:9], v[16:17]
	v_pk_mul_f32 v[10:11], v[10:11], v[0:1]
	s_waitcnt lgkmcnt(0)
	v_sub_f32_e32 v0, v12, v20
	v_sub_f32_e32 v1, v13, v21
	v_mul_f32_e32 v0, 0x3fb8aa3b, v0
	v_mul_f32_e32 v1, 0x3fb8aa3b, v1
	v_exp_f32_e32 v0, v0
	v_exp_f32_e32 v1, v1
	v_lshlrev_b32_e32 v12, 16, v2
	v_and_b32_e32 v13, 0xffff0000, v2
	v_lshlrev_b32_e32 v2, 16, v3
	v_pk_mul_f32 v[12:13], v[0:1], v[12:13]
	v_sub_f32_e32 v0, v14, v22
	v_sub_f32_e32 v1, v15, v23
	v_mul_f32_e32 v0, 0x3fb8aa3b, v0
	v_mul_f32_e32 v1, 0x3fb8aa3b, v1
	v_exp_f32_e32 v0, v0
	v_exp_f32_e32 v1, v1
	v_and_b32_e32 v3, 0xffff0000, v3
	v_pk_mul_f32 v[14:15], v[0:1], v[2:3]
	v_cvt_pk_bf16_f32 v0, v8, v9
	v_cvt_pk_bf16_f32 v1, v10, v11
	v_cvt_pk_bf16_f32 v2, v12, v13
	v_cvt_pk_bf16_f32 v3, v14, v15
	ds_write_b128 v44, v[0:3] offset:33792
	ds_read_b128 v[0:3], v43 offset:32
	ds_read_b128 v[8:11], v43 offset:48
	ds_read_b128 v[12:15], v42 offset:32
	ds_read_b128 v[16:19], v42 offset:48
	s_waitcnt lgkmcnt(1)
	v_sub_f32_e32 v2, v2, v14
	v_sub_f32_e32 v3, v3, v15
	v_mul_f32_e32 v2, 0x3fb8aa3b, v2
	v_mul_f32_e32 v3, 0x3fb8aa3b, v3
	v_exp_f32_e32 v2, v2
	v_exp_f32_e32 v3, v3
	v_sub_f32_e32 v0, v0, v12
	v_sub_f32_e32 v1, v1, v13
	s_waitcnt vmcnt(0)
	v_lshlrev_b32_e32 v12, 16, v4
	v_and_b32_e32 v13, 0xffff0000, v4
	v_lshlrev_b32_e32 v4, 16, v5
	v_and_b32_e32 v5, 0xffff0000, v5
	v_pk_mul_f32 v[2:3], v[2:3], v[4:5]
	s_waitcnt lgkmcnt(0)
	v_sub_f32_e32 v4, v8, v16
	v_sub_f32_e32 v5, v9, v17
	v_mul_f32_e32 v4, 0x3fb8aa3b, v4
	v_mul_f32_e32 v5, 0x3fb8aa3b, v5
	v_exp_f32_e32 v4, v4
	v_exp_f32_e32 v5, v5
	v_lshlrev_b32_e32 v8, 16, v6
	v_and_b32_e32 v9, 0xffff0000, v6
	v_sub_f32_e32 v6, v10, v18
	v_mul_f32_e32 v6, 0x3fb8aa3b, v6
	v_pk_mul_f32 v[4:5], v[4:5], v[8:9]
	v_exp_f32_e32 v8, v6
	v_sub_f32_e32 v6, v11, v19
	v_mul_f32_e32 v0, 0x3fb8aa3b, v0
	v_mul_f32_e32 v1, 0x3fb8aa3b, v1
	v_mul_f32_e32 v6, 0x3fb8aa3b, v6
	v_exp_f32_e32 v0, v0
	v_exp_f32_e32 v1, v1
	v_exp_f32_e32 v9, v6
	v_lshlrev_b32_e32 v6, 16, v7
	v_and_b32_e32 v7, 0xffff0000, v7
	v_pk_mul_f32 v[0:1], v[0:1], v[12:13]
	v_pk_mul_f32 v[6:7], v[8:9], v[6:7]
	v_cvt_pk_bf16_f32 v0, v0, v1
	v_cvt_pk_bf16_f32 v1, v2, v3
	v_cvt_pk_bf16_f32 v2, v4, v5
	v_cvt_pk_bf16_f32 v3, v6, v7
	ds_write_b128 v44, v[0:3] offset:33808
	v_lshl_add_u64 v[0:1], v[36:37], 0, s[50:51]
	v_lshl_add_u64 v[0:1], v[0:1], 0, v[34:35]
	v_lshl_add_u64 v[12:13], v[0:1], 0, s[10:11]
	v_add_co_u32_e64 v0, s[10:11], s12, v0
	s_nop 1
	v_addc_co_u32_e64 v1, s[10:11], 0, v1, s[10:11]
	s_waitcnt vmcnt(0)
	ds_write_b128 v45, v[136:139] offset:51200
	ds_write_b128 v45, v[140:143] offset:51216
	ds_write_b128 v45, v[144:147] offset:51232
	ds_write_b128 v45, v[148:151] offset:51248
	s_and_saveexec_b64 s[10:11], s[8:9]
	s_xor_b64 s[10:11], exec, s[10:11]
	s_lshl_b32 s12, s22, 5
	s_or_b32 s12, s12, s26
	s_ashr_i32 s13, s12, 31
	s_or_saveexec_b64 s[10:11], s[10:11]
	v_mov_b64_e32 v[0:1], s[12:13]
	s_xor_b64 exec, exec, s[10:11]
	s_cbranch_execz .LBB0_640
	ds_read_b32 v0, v46
	s_lshl_b32 s12, s22, 5
	s_or_b32 s12, s12, s26
	s_ashr_i32 s13, s12, 31
	s_lshl_b64 s[22:23], s[12:13], 9
	s_waitcnt lgkmcnt(0)
	v_mul_f32_e32 v0, 0x3fb8aa3b, v0
	v_exp_f32_e32 v2, v0
	v_lshl_add_u64 v[0:1], v[28:29], 0, s[22:23]
	global_store_dword v[0:1], v2, off
	v_mov_b64_e32 v[0:1], s[12:13]
	s_branch .LBB0_640

.LBB0_766:
	s_ashr_i32 s30, s91, 7
	s_and_b32 s84, s91, 31
	s_ashr_i32 s31, s30, 31
	s_lshl_b64 s[42:43], s[30:31], 11
	s_lshl_b32 s28, s84, 6
	s_or_b32 s42, s42, s28
	v_lshl_add_u64 v[24:25], s[42:43], 0, v[42:43]
	v_mov_b64_e32 v[0:1], s[62:63]
	s_bfe_u32 s85, s91, 0x20005
	v_mad_u64_u32 v[0:1], s[30:31], v24, s48, v[0:1]
	v_mad_i32_i24 v1, v25, s48, v1
	s_lshl_b32 s50, s85, 8
	v_lshl_add_u64 v[0:1], v[0:1], 0, s[50:51]
	v_lshl_add_u64 v[0:1], v[0:1], 0, v[208:209]
	s_mov_b64 s[30:31], 0x3d902800
	s_mov_b32 s28, 0x3d902000
	v_lshl_add_u64 v[2:3], v[0:1], 0, s[30:31]
	s_lshl_b32 s60, s85, 9
	s_mov_b32 s61, s51
	v_add_co_u32_e32 v0, vcc, s28, v0
	v_lshl_add_u64 v[20:21], v[44:45], 0, s[60:61]
	s_nop 0
	v_addc_co_u32_e32 v1, vcc, 0, v1, vcc
	global_load_dwordx4 v[12:15], v[0:1], off offset:2048
	s_nop 0
	global_load_dwordx4 v[0:3], v[2:3], off offset:16
	s_nop 0
	global_load_dwordx4 v[4:7], v[20:21], off offset:48
	global_load_dwordx4 v[8:11], v[20:21], off offset:32
	global_load_dwordx4 v[16:19], v[20:21], off offset:16
	s_nop 0
	global_load_dwordx4 v[20:23], v[20:21], off
	v_mad_u64_u32 v[184:185], vcc, v24, s48, 0
	v_mad_i32_i24 v185, v25, s48, v185
	v_lshl_add_u64 v[184:185], s[74:75], 0, v[184:185]
	v_mov_b32_e32 v186, s85
	v_lshlrev_b32_e32 v186, 8, v186
	v_mov_b32_e32 v187, v209
	v_lshl_add_u64 v[188:189], v[184:185], 0, v[186:187]
	v_mov_b32_e32 v190, v56
	v_mov_b32_e32 v191, v209
	v_lshl_add_u64 v[188:189], v[188:189], 0, v[190:191]
	v_lshl_add_u64 v[188:189], v[188:189], 0, s[70:71]
	global_load_dwordx4 v[168:171], v[188:189], off
	global_load_dwordx4 v[172:175], v[188:189], off offset:16
	global_load_dwordx4 v[176:179], v[188:189], off offset:1024
	global_load_dwordx4 v[180:183], v[188:189], off offset:1040
	v_lshl_add_u64 v[192:193], v[184:185], 0, s[60:61]
	v_mov_b32_e32 v190, v58
	v_lshl_add_u64 v[192:193], v[192:193], 0, v[190:191]
	v_add_co_u32_e32 v192, vcc, 0x1800, v192
	s_nop 1
	v_addc_co_u32_e32 v193, vcc, 0, v193, vcc
	global_load_dwordx4 v[128:131], v[192:193], off
	global_load_dwordx4 v[140:143], v[192:193], off offset:16
	global_load_dwordx4 v[136:139], v[192:193], off offset:32
	global_load_dwordx4 v[132:135], v[192:193], off offset:48
	s_and_b32 s30, s91, 0xffffff80
	s_lshl_b32 s31, s85, 5
	s_or_b32 s30, s31, s30
	s_or_b32 s30, s30, s84
	s_ashr_i32 s31, s30, 31
	s_lshl_b64 s[30:31], s[30:31], 16
	v_lshl_add_u64 v[194:195], v[46:47], 0, s[30:31]
	global_load_dwordx4 v[156:159], v[194:195], off
	global_load_dwordx4 v[152:155], v[194:195], off offset:16
	global_load_dwordx4 v[148:151], v[194:195], off offset:32
	global_load_dwordx4 v[144:147], v[194:195], off offset:48
	s_waitcnt vmcnt(17)
	v_lshlrev_b32_e32 v26, 16, v12
	v_and_b32_e32 v12, 0xffff0000, v12
	s_waitcnt vmcnt(12)
	v_add_f32_e32 v26, v20, v26
	v_min_f32_e32 v20, 0, v26
	v_mul_f32_e64 v26, |v26|, s89
	v_exp_f32_e32 v26, v26
	v_add_f32_e32 v12, v21, v12
	v_min_f32_e32 v21, 0, v12
	v_mul_f32_e64 v12, |v12|, s89
	v_add_f32_e32 v26, 1.0, v26
	v_cmp_gt_f32_e32 vcc, s33, v26
	v_exp_f32_e32 v12, v12
	s_nop 0
	v_cndmask_b32_e64 v27, 0, 32, vcc
	v_ldexp_f32 v26, v26, v27
	v_log_f32_e32 v26, v26
	v_add_f32_e32 v12, 1.0, v12
	v_mul_f32_e32 v27, 0x3f317217, v26
	v_fma_f32 v27, v26, s83, -v27
	v_fmac_f32_e32 v27, 0x3377d1cf, v26
	v_fmac_f32_e32 v27, 0x3f317217, v26
	v_cmp_lt_f32_e64 s[30:31], |v26|, s93
	s_nop 1
	v_cndmask_b32_e64 v26, v26, v27, s[30:31]
	v_cndmask_b32_e32 v27, 0, v241, vcc
	v_cmp_gt_f32_e32 vcc, s33, v12
	v_sub_f32_e32 v26, v26, v27
	s_nop 0
	v_cndmask_b32_e64 v27, 0, 32, vcc
	v_ldexp_f32 v12, v12, v27
	v_log_f32_e32 v12, v12
	s_nop 0
	v_mul_f32_e32 v27, 0x3f317217, v12
	v_fma_f32 v27, v12, s83, -v27
	v_fmac_f32_e32 v27, 0x3377d1cf, v12
	v_fmac_f32_e32 v27, 0x3f317217, v12
	v_cmp_lt_f32_e64 s[30:31], |v12|, s93
	s_nop 1
	v_cndmask_b32_e64 v12, v12, v27, s[30:31]
	v_cndmask_b32_e32 v27, 0, v241, vcc
	v_sub_f32_e32 v27, v12, v27
	v_lshlrev_b32_e32 v12, 16, v13
	v_add_f32_e32 v22, v22, v12
	v_min_f32_e32 v12, 0, v22
	v_mul_f32_e64 v22, |v22|, s89
	v_exp_f32_e32 v22, v22
	v_pk_add_f32 v[20:21], v[20:21], v[26:27] neg_lo:[0,1] neg_hi:[0,1]
	v_and_b32_e32 v13, 0xffff0000, v13
	v_add_f32_e32 v23, v23, v13
	v_add_f32_e32 v22, 1.0, v22
	v_cmp_gt_f32_e32 vcc, s33, v22
	v_min_f32_e32 v13, 0, v23
	v_mul_f32_e64 v23, |v23|, s89
	v_cndmask_b32_e64 v26, 0, 32, vcc
	v_ldexp_f32 v22, v22, v26
	v_log_f32_e32 v22, v22
	v_exp_f32_e32 v23, v23
	v_pk_mul_f32 v[20:21], v[20:21], s[76:77] op_sel_hi:[1,0]
	v_mul_f32_e32 v26, 0x3f317217, v22
	v_fma_f32 v26, v22, s83, -v26
	v_fmac_f32_e32 v26, 0x3377d1cf, v22
	v_fmac_f32_e32 v26, 0x3f317217, v22
	v_cmp_lt_f32_e64 s[30:31], |v22|, s93
	v_add_f32_e32 v23, 1.0, v23
	s_nop 0
	v_cndmask_b32_e64 v22, v22, v26, s[30:31]
	v_cndmask_b32_e32 v26, 0, v241, vcc
	v_cmp_gt_f32_e32 vcc, s33, v23
	v_sub_f32_e32 v22, v22, v26
	s_nop 0
	v_cndmask_b32_e64 v26, 0, 32, vcc
	v_ldexp_f32 v23, v23, v26
	v_log_f32_e32 v23, v23
	s_nop 0
	v_mul_f32_e32 v26, 0x3f317217, v23
	v_fma_f32 v26, v23, s83, -v26
	v_fmac_f32_e32 v26, 0x3377d1cf, v23
	v_fmac_f32_e32 v26, 0x3f317217, v23
	v_cmp_lt_f32_e64 s[30:31], |v23|, s93
	s_nop 1
	v_cndmask_b32_e64 v23, v23, v26, s[30:31]
	v_cndmask_b32_e32 v26, 0, v241, vcc
	v_sub_f32_e32 v23, v23, v26
	v_pk_add_f32 v[12:13], v[12:13], v[22:23] neg_lo:[0,1] neg_hi:[0,1]
	v_mov_b32_e32 v26, 0
	v_pk_mul_f32 v[22:23], v[12:13], s[76:77] op_sel_hi:[1,0]
	v_lshlrev_b32_e32 v12, 16, v14
	v_add_f32_e32 v13, v16, v12
	v_min_f32_e32 v12, 0, v13
	v_mul_f32_e64 v13, |v13|, s89
	v_exp_f32_e32 v13, v13
	ds_write_b128 v41, v[20:23]
	v_add_u32_e32 v20, 0x1c00, v119
	v_add_f32_e32 v13, 1.0, v13
	v_cmp_gt_f32_e32 vcc, s33, v13
	s_nop 1
	v_cndmask_b32_e64 v16, 0, 32, vcc
	v_ldexp_f32 v13, v13, v16
	v_log_f32_e32 v13, v13
	s_nop 0
	v_mul_f32_e32 v16, 0x3f317217, v13
	v_fma_f32 v16, v13, s83, -v16
	v_fmac_f32_e32 v16, 0x3377d1cf, v13
	v_fmac_f32_e32 v16, 0x3f317217, v13
	v_cmp_lt_f32_e64 s[30:31], |v13|, s93
	s_nop 1
	v_cndmask_b32_e64 v13, v13, v16, s[30:31]
	v_cndmask_b32_e32 v16, 0, v241, vcc
	v_sub_f32_e32 v16, v13, v16
	v_and_b32_e32 v13, 0xffff0000, v14
	v_add_f32_e32 v14, v17, v13
	v_min_f32_e32 v13, 0, v14
	v_mul_f32_e64 v14, |v14|, s89
	v_exp_f32_e32 v14, v14
	s_nop 0
	v_add_f32_e32 v14, 1.0, v14
	v_cmp_gt_f32_e32 vcc, s33, v14
	s_nop 1
	v_cndmask_b32_e64 v17, 0, 32, vcc
	v_ldexp_f32 v14, v14, v17
	v_log_f32_e32 v14, v14
	s_nop 0
	v_mul_f32_e32 v17, 0x3f317217, v14
	v_fma_f32 v17, v14, s83, -v17
	v_fmac_f32_e32 v17, 0x3377d1cf, v14
	v_fmac_f32_e32 v17, 0x3f317217, v14
	v_cmp_lt_f32_e64 s[30:31], |v14|, s93
	s_nop 1
	v_cndmask_b32_e64 v14, v14, v17, s[30:31]
	v_cndmask_b32_e32 v17, 0, v241, vcc
	v_sub_f32_e32 v17, v14, v17
	v_lshlrev_b32_e32 v14, 16, v15
	v_pk_add_f32 v[12:13], v[12:13], v[16:17] neg_lo:[0,1] neg_hi:[0,1]
	v_add_f32_e32 v16, v18, v14
	v_min_f32_e32 v14, 0, v16
	v_mul_f32_e64 v16, |v16|, s89
	v_exp_f32_e32 v16, v16
	v_and_b32_e32 v15, 0xffff0000, v15
	v_pk_mul_f32 v[12:13], v[12:13], s[76:77] op_sel_hi:[1,0]
	v_add_f32_e32 v16, 1.0, v16
	v_cmp_gt_f32_e32 vcc, s33, v16
	s_nop 1
	v_cndmask_b32_e64 v17, 0, 32, vcc
	v_ldexp_f32 v16, v16, v17
	v_log_f32_e32 v16, v16
	s_nop 0
	v_mul_f32_e32 v17, 0x3f317217, v16
	v_fma_f32 v17, v16, s83, -v17
	v_fmac_f32_e32 v17, 0x3377d1cf, v16
	v_fmac_f32_e32 v17, 0x3f317217, v16
	v_cmp_lt_f32_e64 s[30:31], |v16|, s93
	s_nop 1
	v_cndmask_b32_e64 v16, v16, v17, s[30:31]
	v_cndmask_b32_e32 v17, 0, v241, vcc
	v_sub_f32_e32 v16, v16, v17
	v_add_f32_e32 v17, v19, v15
	v_min_f32_e32 v15, 0, v17
	v_mul_f32_e64 v17, |v17|, s89
	v_exp_f32_e32 v17, v17
	s_nop 0
	v_add_f32_e32 v17, 1.0, v17
	v_cmp_gt_f32_e32 vcc, s33, v17
	s_nop 1
	v_cndmask_b32_e64 v18, 0, 32, vcc
	v_ldexp_f32 v17, v17, v18
	v_log_f32_e32 v17, v17
	s_nop 0
	v_mul_f32_e32 v18, 0x3f317217, v17
	v_fma_f32 v18, v17, s83, -v18
	v_fmac_f32_e32 v18, 0x3377d1cf, v17
	v_fmac_f32_e32 v18, 0x3f317217, v17
	v_cmp_lt_f32_e64 s[30:31], |v17|, s93
	s_nop 1
	v_cndmask_b32_e64 v17, v17, v18, s[30:31]
	v_cndmask_b32_e32 v18, 0, v241, vcc
	v_sub_f32_e32 v17, v17, v18
	v_pk_add_f32 v[14:15], v[14:15], v[16:17] neg_lo:[0,1] neg_hi:[0,1]
	s_nop 0
	v_pk_mul_f32 v[14:15], v[14:15], s[76:77] op_sel_hi:[1,0]
	ds_write_b128 v41, v[12:15] offset:16
	v_lshlrev_b32_e32 v12, 16, v0
	v_add_f32_e32 v12, v8, v12
	v_min_f32_e32 v8, 0, v12
	v_mul_f32_e64 v12, |v12|, s89
	v_exp_f32_e32 v12, v12
	v_and_b32_e32 v0, 0xffff0000, v0
	v_add_f32_e32 v0, v9, v0
	v_min_f32_e32 v9, 0, v0
	v_add_f32_e32 v12, 1.0, v12
	v_cmp_gt_f32_e32 vcc, s33, v12
	v_mul_f32_e64 v0, |v0|, s89
	v_exp_f32_e32 v0, v0
	v_cndmask_b32_e64 v13, 0, 32, vcc
	v_ldexp_f32 v12, v12, v13
	v_log_f32_e32 v12, v12
	v_add_f32_e32 v0, 1.0, v0
	v_mul_f32_e32 v13, 0x3f317217, v12
	v_fma_f32 v13, v12, s83, -v13
	v_fmac_f32_e32 v13, 0x3377d1cf, v12
	v_fmac_f32_e32 v13, 0x3f317217, v12
	v_cmp_lt_f32_e64 s[30:31], |v12|, s93
	s_nop 1
	v_cndmask_b32_e64 v12, v12, v13, s[30:31]
	v_cndmask_b32_e32 v13, 0, v241, vcc
	v_cmp_gt_f32_e32 vcc, s33, v0
	v_sub_f32_e32 v12, v12, v13
	s_nop 0
	v_cndmask_b32_e64 v13, 0, 32, vcc
	v_ldexp_f32 v0, v0, v13
	v_log_f32_e32 v0, v0
	s_nop 0
	v_mul_f32_e32 v13, 0x3f317217, v0
	v_fma_f32 v13, v0, s83, -v13
	v_fmac_f32_e32 v13, 0x3377d1cf, v0
	v_fmac_f32_e32 v13, 0x3f317217, v0
	v_cmp_lt_f32_e64 s[30:31], |v0|, s93
	s_nop 1
	v_cndmask_b32_e64 v0, v0, v13, s[30:31]
	v_cndmask_b32_e32 v13, 0, v241, vcc
	v_sub_f32_e32 v13, v0, v13
	v_lshlrev_b32_e32 v0, 16, v1
	v_add_f32_e32 v10, v10, v0
	v_min_f32_e32 v0, 0, v10
	v_mul_f32_e64 v10, |v10|, s89
	v_exp_f32_e32 v10, v10
	v_pk_add_f32 v[8:9], v[8:9], v[12:13] neg_lo:[0,1] neg_hi:[0,1]
	v_and_b32_e32 v1, 0xffff0000, v1
	v_add_f32_e32 v11, v11, v1
	v_add_f32_e32 v10, 1.0, v10
	v_cmp_gt_f32_e32 vcc, s33, v10
	v_min_f32_e32 v1, 0, v11
	v_mul_f32_e64 v11, |v11|, s89
	v_cndmask_b32_e64 v12, 0, 32, vcc
	v_ldexp_f32 v10, v10, v12
	v_log_f32_e32 v10, v10
	v_exp_f32_e32 v11, v11
	v_pk_mul_f32 v[8:9], v[8:9], s[76:77] op_sel_hi:[1,0]
	v_mul_f32_e32 v12, 0x3f317217, v10
	v_fma_f32 v12, v10, s83, -v12
	v_fmac_f32_e32 v12, 0x3377d1cf, v10
	v_fmac_f32_e32 v12, 0x3f317217, v10
	v_cmp_lt_f32_e64 s[30:31], |v10|, s93
	v_add_f32_e32 v11, 1.0, v11
	s_nop 0
	v_cndmask_b32_e64 v10, v10, v12, s[30:31]
	v_cndmask_b32_e32 v12, 0, v241, vcc
	v_cmp_gt_f32_e32 vcc, s33, v11
	v_sub_f32_e32 v10, v10, v12
	s_nop 0
	v_cndmask_b32_e64 v12, 0, 32, vcc
	v_ldexp_f32 v11, v11, v12
	v_log_f32_e32 v11, v11
	s_nop 0
	v_mul_f32_e32 v12, 0x3f317217, v11
	v_fma_f32 v12, v11, s83, -v12
	v_fmac_f32_e32 v12, 0x3377d1cf, v11
	v_fmac_f32_e32 v12, 0x3f317217, v11
	v_cmp_lt_f32_e64 s[30:31], |v11|, s93
	s_nop 1
	v_cndmask_b32_e64 v11, v11, v12, s[30:31]
	v_cndmask_b32_e32 v12, 0, v241, vcc
	v_sub_f32_e32 v11, v11, v12
	v_pk_add_f32 v[0:1], v[0:1], v[10:11] neg_lo:[0,1] neg_hi:[0,1]
	v_add_u32_e32 v12, 0x1400, v119
	v_pk_mul_f32 v[10:11], v[0:1], s[76:77] op_sel_hi:[1,0]
	v_lshlrev_b32_e32 v0, 16, v2
	v_add_f32_e32 v1, v4, v0
	v_min_f32_e32 v0, 0, v1
	v_mul_f32_e64 v1, |v1|, s89
	v_exp_f32_e32 v1, v1
	ds_write_b128 v41, v[8:11] offset:32
	v_add_u32_e32 v8, 0xc00, v119
	v_add_f32_e32 v1, 1.0, v1
	v_cmp_gt_f32_e32 vcc, s33, v1
	s_nop 1
	v_cndmask_b32_e64 v4, 0, 32, vcc
	v_ldexp_f32 v1, v1, v4
	v_log_f32_e32 v1, v1
	s_nop 0
	v_mul_f32_e32 v4, 0x3f317217, v1
	v_fma_f32 v4, v1, s83, -v4
	v_fmac_f32_e32 v4, 0x3377d1cf, v1
	v_fmac_f32_e32 v4, 0x3f317217, v1
	v_cmp_lt_f32_e64 s[30:31], |v1|, s93
	s_nop 1
	v_cndmask_b32_e64 v1, v1, v4, s[30:31]
	v_cndmask_b32_e32 v4, 0, v241, vcc
	v_sub_f32_e32 v4, v1, v4
	v_and_b32_e32 v1, 0xffff0000, v2
	v_add_f32_e32 v2, v5, v1
	v_min_f32_e32 v1, 0, v2
	v_mul_f32_e64 v2, |v2|, s89
	v_exp_f32_e32 v2, v2
	s_nop 0
	v_add_f32_e32 v2, 1.0, v2
	v_cmp_gt_f32_e32 vcc, s33, v2
	s_nop 1
	v_cndmask_b32_e64 v5, 0, 32, vcc
	v_ldexp_f32 v2, v2, v5
	v_log_f32_e32 v2, v2
	s_nop 0
	v_mul_f32_e32 v5, 0x3f317217, v2
	v_fma_f32 v5, v2, s83, -v5
	v_fmac_f32_e32 v5, 0x3377d1cf, v2
	v_fmac_f32_e32 v5, 0x3f317217, v2
	v_cmp_lt_f32_e64 s[30:31], |v2|, s93
	s_nop 1
	v_cndmask_b32_e64 v2, v2, v5, s[30:31]
	v_cndmask_b32_e32 v5, 0, v241, vcc
	v_sub_f32_e32 v5, v2, v5
	v_lshlrev_b32_e32 v2, 16, v3
	v_pk_add_f32 v[0:1], v[0:1], v[4:5] neg_lo:[0,1] neg_hi:[0,1]
	v_add_f32_e32 v4, v6, v2
	v_min_f32_e32 v2, 0, v4
	v_mul_f32_e64 v4, |v4|, s89
	v_exp_f32_e32 v4, v4
	v_and_b32_e32 v3, 0xffff0000, v3
	v_pk_mul_f32 v[0:1], v[0:1], s[76:77] op_sel_hi:[1,0]
	v_add_f32_e32 v4, 1.0, v4
	v_cmp_gt_f32_e32 vcc, s33, v4
	s_nop 1
	v_cndmask_b32_e64 v5, 0, 32, vcc
	v_ldexp_f32 v4, v4, v5
	v_log_f32_e32 v4, v4
	s_nop 0
	v_mul_f32_e32 v5, 0x3f317217, v4
	v_fma_f32 v5, v4, s83, -v5
	v_fmac_f32_e32 v5, 0x3377d1cf, v4
	v_fmac_f32_e32 v5, 0x3f317217, v4
	v_cmp_lt_f32_e64 s[30:31], |v4|, s93
	s_nop 1
	v_cndmask_b32_e64 v4, v4, v5, s[30:31]
	v_cndmask_b32_e32 v5, 0, v241, vcc
	v_sub_f32_e32 v4, v4, v5
	v_add_f32_e32 v5, v7, v3
	v_min_f32_e32 v3, 0, v5
	v_mul_f32_e64 v5, |v5|, s89
	v_exp_f32_e32 v5, v5
	s_nop 0
	v_add_f32_e32 v5, 1.0, v5
	v_cmp_gt_f32_e32 vcc, s33, v5
	s_nop 1
	v_cndmask_b32_e64 v6, 0, 32, vcc
	v_ldexp_f32 v5, v5, v6
	v_log_f32_e32 v5, v5
	s_nop 0
	v_mul_f32_e32 v6, 0x3f317217, v5
	v_fma_f32 v6, v5, s83, -v6
	v_fmac_f32_e32 v6, 0x3377d1cf, v5
	v_fmac_f32_e32 v6, 0x3f317217, v5
	v_cmp_lt_f32_e64 s[30:31], |v5|, s93
	s_nop 1
	v_cndmask_b32_e64 v5, v5, v6, s[30:31]
	v_cndmask_b32_e32 v6, 0, v241, vcc
	v_sub_f32_e32 v5, v5, v6
	v_pk_add_f32 v[2:3], v[2:3], v[4:5] neg_lo:[0,1] neg_hi:[0,1]
	s_nop 0
	v_pk_mul_f32 v[2:3], v[2:3], s[76:77] op_sel_hi:[1,0]
	ds_write_b128 v41, v[0:3] offset:48
	s_waitcnt lgkmcnt(0)
	s_barrier
	ds_read2_b32 v[0:1], v119 offset1:132
	v_add_u32_e32 v2, 0x400, v119
	ds_read2_b32 v[4:5], v2 offset0:8 offset1:140
	v_add_u32_e32 v3, 0x800, v119
	ds_read2_b32 v[6:7], v3 offset0:16 offset1:148
	s_waitcnt lgkmcnt(2)
	v_add_f32_e32 v0, 0, v0
	v_add_f32_e32 v1, v0, v1
	ds_read2_b32 v[10:11], v8 offset0:24 offset1:156
	s_waitcnt lgkmcnt(2)
	v_add_f32_e32 v4, v1, v4
	v_add_f32_e32 v5, v4, v5
	s_waitcnt lgkmcnt(1)
	v_add_f32_e32 v6, v5, v6
	v_add_f32_e32 v7, v6, v7
	s_waitcnt lgkmcnt(0)
	v_add_f32_e32 v9, v7, v10
	v_add_f32_e32 v10, v9, v11
	v_add_u32_e32 v11, 0x1000, v119
	ds_read2_b32 v[14:15], v11 offset0:32 offset1:164
	ds_read2_b32 v[16:17], v12 offset0:40 offset1:172
	ds_read2_b32 v[22:23], v20 offset0:56 offset1:188
	s_waitcnt lgkmcnt(2)
	v_add_f32_e32 v13, v10, v14
	v_add_f32_e32 v14, v13, v15
	s_waitcnt lgkmcnt(1)
	v_add_f32_e32 v15, v14, v16
	v_add_f32_e32 v16, v15, v17
	v_add_u32_e32 v17, 0x1800, v119
	ds_read2_b32 v[18:19], v17 offset0:48 offset1:180
	s_waitcnt lgkmcnt(0)
	v_add_f32_e32 v18, v16, v18
	v_add_f32_e32 v19, v18, v19
	v_add_f32_e32 v21, v19, v22
	v_add_f32_e32 v22, v21, v23
	v_mov_b32_e32 v23, 0
	ds_write_b32 v49, v22
	s_waitcnt lgkmcnt(0)
	s_barrier
	s_and_saveexec_b64 s[30:31], s[2:3]
	s_cbranch_execz .LBB0_784
	ds_read_b32 v26, v51
	s_waitcnt lgkmcnt(0)
	v_add_f32_e32 v26, 0, v26
	s_or_b64 exec, exec, s[30:31]
	v_mov_b32_e32 v27, 0
	s_and_saveexec_b64 s[30:31], s[4:5]
	s_cbranch_execnz .LBB0_785

.LBB0_770:
	s_or_b64 exec, exec, s[30:31]
	s_waitcnt lgkmcnt(0)
	v_add_f32_e32 v26, v26, v27
	v_add_f32_e32 v23, v26, v23
	v_add_f32_e32 v0, v0, v23
	v_add_f32_e32 v1, v1, v23
	ds_write2_b32 v119, v0, v1 offset1:132
	v_add_f32_e32 v0, v4, v23
	v_add_f32_e32 v1, v5, v23
	ds_write2_b32 v2, v0, v1 offset0:8 offset1:140
	v_add_f32_e32 v0, v6, v23
	v_add_f32_e32 v1, v7, v23
	ds_write2_b32 v3, v0, v1 offset0:16 offset1:148
	v_add_f32_e32 v0, v9, v23
	v_add_f32_e32 v1, v10, v23
	ds_write2_b32 v8, v0, v1 offset0:24 offset1:156
	v_add_f32_e32 v0, v13, v23
	v_add_f32_e32 v1, v14, v23
	ds_write2_b32 v11, v0, v1 offset0:32 offset1:164
	v_add_f32_e32 v0, v15, v23
	v_add_f32_e32 v1, v16, v23
	ds_write2_b32 v12, v0, v1 offset0:40 offset1:172
	v_add_f32_e32 v0, v18, v23
	v_add_f32_e32 v1, v19, v23
	s_lshl_b32 s28, s85, 7
	ds_write2_b32 v17, v0, v1 offset0:48 offset1:180
	v_add_f32_e32 v1, v21, v23
	v_add_f32_e32 v0, v22, v23
	ds_write2_b32 v20, v1, v0 offset0:56 offset1:188
	s_and_saveexec_b64 s[30:31], s[8:9]
	ds_write_b32 v53, v0
	s_or_b64 exec, exec, s[30:31]
	v_mad_u64_u32 v[0:1], s[30:31], v24, s48, 0
	v_mad_i32_i24 v1, v25, s48, v1
	v_lshl_add_u64 v[16:17], s[74:75], 0, v[0:1]
	s_lshl_b32 s64, s28, 1
	s_mov_b32 s65, s51
	v_mov_b32_e32 v57, v209
	v_lshl_add_u64 v[0:1], v[16:17], 0, s[64:65]
	v_lshl_add_u64 v[0:1], v[0:1], 0, v[56:57]
	s_movk_i32 s28, 0x1000
	s_mov_b64 s[64:65], 0x1400
	v_add_co_u32_e32 v6, vcc, s28, v0
	v_lshl_add_u64 v[2:3], v[0:1], 0, s[70:71]
	v_lshl_add_u64 v[4:5], v[0:1], 0, s[64:65]
	v_addc_co_u32_e32 v7, vcc, 0, v1, vcc
	s_waitcnt lgkmcnt(0)
	s_barrier
	s_waitcnt vmcnt(0)
	v_mov_b32_e32 v24, v168
	v_mov_b32_e32 v25, v169
	v_mov_b32_e32 v26, v170
	v_mov_b32_e32 v27, v171
	v_mov_b32_e32 v0, v172
	v_mov_b32_e32 v1, v173
	v_mov_b32_e32 v2, v174
	v_mov_b32_e32 v3, v175
	v_mov_b32_e32 v8, v176
	v_mov_b32_e32 v9, v177
	v_mov_b32_e32 v10, v178
	v_mov_b32_e32 v11, v179
	v_mov_b32_e32 v4, v180
	v_mov_b32_e32 v5, v181
	v_mov_b32_e32 v6, v182
	v_mov_b32_e32 v7, v183
	ds_read_b128 v[28:31], v104
	ds_read_b128 v[12:15], v104 offset:16
	s_mov_b32 s61, s51
	v_mov_b32_e32 v59, v209
	s_and_b32 s30, s91, 0xffffff80
	s_waitcnt lgkmcnt(1)
	v_mul_f32_e32 v19, 0xbfb8aa3b, v28
	v_mul_f32_e32 v18, 0x3fb8aa3b, v28
	v_exp_f32_e32 v20, v19
	v_mul_f32_e32 v19, 0x3fb8aa3b, v29
	v_exp_f32_e32 v18, v18
	v_exp_f32_e32 v19, v19
	v_mul_f32_e32 v21, 0xbfb8aa3b, v29
	v_exp_f32_e32 v21, v21
	s_lshl_b32 s31, s85, 5
	s_or_b32 s30, s31, s30
	s_or_b32 s30, s30, s84
	s_ashr_i32 s31, s30, 31
	s_lshl_b64 s[30:31], s[30:31], 16
	s_waitcnt vmcnt(3)
	v_lshlrev_b32_e32 v22, 16, v24
	v_and_b32_e32 v23, 0xffff0000, v24
	v_pk_mul_f32 v[22:23], v[22:23], s[86:87] op_sel_hi:[1,0]
	v_lshlrev_b32_e32 v28, 16, v25
	v_pk_mul_f32 v[18:19], v[22:23], v[18:19]
	s_waitcnt vmcnt(1)
	v_lshlrev_b32_e32 v22, 16, v8
	v_and_b32_e32 v23, 0xffff0000, v8
	v_mul_f32_e32 v8, 0x3fb8aa3b, v30
	v_pk_mul_f32 v[20:21], v[20:21], v[22:23]
	v_exp_f32_e32 v22, v8
	v_mul_f32_e32 v8, 0xbfb8aa3b, v30
	v_exp_f32_e32 v24, v8
	v_mul_f32_e32 v8, 0x3fb8aa3b, v31
	v_exp_f32_e32 v23, v8
	v_mul_f32_e32 v8, 0xbfb8aa3b, v31
	v_and_b32_e32 v29, 0xffff0000, v25
	v_exp_f32_e32 v25, v8
	v_lshlrev_b32_e32 v8, 16, v9
	v_and_b32_e32 v9, 0xffff0000, v9
	v_pk_mul_f32 v[28:29], v[28:29], s[86:87] op_sel_hi:[1,0]
	v_pk_mul_f32 v[8:9], v[24:25], v[8:9]
	s_waitcnt lgkmcnt(0)
	v_mul_f32_e32 v24, 0x3fb8aa3b, v12
	v_mul_f32_e32 v25, 0x3fb8aa3b, v13
	v_exp_f32_e32 v24, v24
	v_mul_f32_e32 v12, 0xbfb8aa3b, v12
	v_exp_f32_e32 v25, v25
	v_mul_f32_e32 v13, 0xbfb8aa3b, v13
	v_exp_f32_e32 v12, v12
	v_exp_f32_e32 v13, v13
	v_pk_mul_f32 v[22:23], v[28:29], v[22:23]
	v_lshlrev_b32_e32 v28, 16, v26
	v_and_b32_e32 v29, 0xffff0000, v26
	v_pk_mul_f32 v[28:29], v[28:29], s[86:87] op_sel_hi:[1,0]
	v_lshlrev_b32_e32 v26, 16, v27
	v_pk_mul_f32 v[24:25], v[28:29], v[24:25]
	v_lshlrev_b32_e32 v28, 16, v10
	v_and_b32_e32 v29, 0xffff0000, v10
	v_mul_f32_e32 v10, 0x3fb8aa3b, v14
	v_pk_mul_f32 v[28:29], v[12:13], v[28:29]
	v_exp_f32_e32 v12, v10
	v_mul_f32_e32 v10, 0xbfb8aa3b, v14
	v_exp_f32_e32 v14, v10
	v_mul_f32_e32 v10, 0x3fb8aa3b, v15
	v_exp_f32_e32 v13, v10
	v_mul_f32_e32 v10, 0xbfb8aa3b, v15
	v_exp_f32_e32 v15, v10
	v_and_b32_e32 v27, 0xffff0000, v27
	v_pk_mul_f32 v[26:27], v[26:27], s[86:87] op_sel_hi:[1,0]
	v_lshlrev_b32_e32 v10, 16, v11
	v_pk_mul_f32 v[26:27], v[26:27], v[12:13]
	v_and_b32_e32 v11, 0xffff0000, v11
	v_pk_mul_f32 v[14:15], v[14:15], v[10:11]
	v_cvt_pk_bf16_f32 v10, v18, v19
	v_cvt_pk_bf16_f32 v11, v22, v23
	v_cvt_pk_bf16_f32 v12, v24, v25
	v_cvt_pk_bf16_f32 v13, v26, v27
	ds_write_b128 v105, v[10:13] offset:33792
	v_cvt_pk_bf16_f32 v10, v20, v21
	v_cvt_pk_bf16_f32 v11, v8, v9
	v_cvt_pk_bf16_f32 v12, v28, v29
	v_cvt_pk_bf16_f32 v13, v14, v15
	ds_write_b128 v105, v[10:13] offset:51200
	ds_read_b128 v[8:11], v104 offset:32
	ds_read_b128 v[12:15], v104 offset:48
	v_lshlrev_b32_e32 v20, 16, v0
	v_and_b32_e32 v21, 0xffff0000, v0
	v_pk_mul_f32 v[20:21], v[20:21], s[86:87] op_sel_hi:[1,0]
	s_waitcnt lgkmcnt(1)
	v_mul_f32_e32 v18, 0x3fb8aa3b, v8
	v_mul_f32_e32 v19, 0x3fb8aa3b, v9
	v_exp_f32_e32 v18, v18
	v_mul_f32_e32 v8, 0xbfb8aa3b, v8
	v_exp_f32_e32 v19, v19
	v_mul_f32_e32 v0, 0xbfb8aa3b, v9
	v_exp_f32_e32 v8, v8
	v_exp_f32_e32 v9, v0
	v_pk_mul_f32 v[18:19], v[20:21], v[18:19]
	s_waitcnt vmcnt(0)
	v_lshlrev_b32_e32 v20, 16, v4
	v_and_b32_e32 v21, 0xffff0000, v4
	v_mul_f32_e32 v0, 0x3fb8aa3b, v10
	v_pk_mul_f32 v[8:9], v[8:9], v[20:21]
	v_exp_f32_e32 v20, v0
	v_mul_f32_e32 v0, 0xbfb8aa3b, v10
	v_lshlrev_b32_e32 v22, 16, v1
	v_and_b32_e32 v23, 0xffff0000, v1
	v_mul_f32_e32 v1, 0xbfb8aa3b, v11
	v_exp_f32_e32 v0, v0
	v_exp_f32_e32 v1, v1
	v_mul_f32_e32 v4, 0x3fb8aa3b, v11
	v_exp_f32_e32 v21, v4
	v_lshlrev_b32_e32 v4, 16, v5
	v_and_b32_e32 v5, 0xffff0000, v5
	v_pk_mul_f32 v[4:5], v[0:1], v[4:5]
	s_waitcnt lgkmcnt(0)
	v_mul_f32_e32 v1, 0xbfb8aa3b, v12
	v_mul_f32_e32 v0, 0x3fb8aa3b, v12
	v_exp_f32_e32 v10, v1
	v_mul_f32_e32 v1, 0x3fb8aa3b, v13
	v_exp_f32_e32 v0, v0
	v_exp_f32_e32 v1, v1
	v_pk_mul_f32 v[22:23], v[22:23], s[86:87] op_sel_hi:[1,0]
	v_lshlrev_b32_e32 v12, 16, v3
	v_pk_mul_f32 v[20:21], v[22:23], v[20:21]
	v_lshlrev_b32_e32 v22, 16, v2
	v_and_b32_e32 v23, 0xffff0000, v2
	v_pk_mul_f32 v[22:23], v[22:23], s[86:87] op_sel_hi:[1,0]
	v_lshl_add_u64 v[28:29], v[46:47], 0, s[30:31]
	v_pk_mul_f32 v[22:23], v[22:23], v[0:1]
	v_mul_f32_e32 v0, 0xbfb8aa3b, v13
	v_exp_f32_e32 v11, v0
	v_lshlrev_b32_e32 v0, 16, v6
	v_and_b32_e32 v1, 0xffff0000, v6
	v_and_b32_e32 v13, 0xffff0000, v3
	v_pk_mul_f32 v[10:11], v[10:11], v[0:1]
	v_mul_f32_e32 v1, 0xbfb8aa3b, v14
	v_mul_f32_e32 v0, 0x3fb8aa3b, v14
	v_exp_f32_e32 v2, v1
	v_mul_f32_e32 v1, 0x3fb8aa3b, v15
	v_exp_f32_e32 v0, v0
	v_exp_f32_e32 v1, v1
	v_pk_mul_f32 v[12:13], v[12:13], s[86:87] op_sel_hi:[1,0]
	s_mov_b64 s[30:31], 0x8000
	v_pk_mul_f32 v[12:13], v[12:13], v[0:1]
	v_mul_f32_e32 v0, 0xbfb8aa3b, v15
	v_exp_f32_e32 v3, v0
	v_lshlrev_b32_e32 v0, 16, v7
	v_and_b32_e32 v1, 0xffff0000, v7
	v_pk_mul_f32 v[6:7], v[2:3], v[0:1]
	v_cvt_pk_bf16_f32 v0, v18, v19
	v_cvt_pk_bf16_f32 v1, v20, v21
	v_cvt_pk_bf16_f32 v2, v22, v23
	v_cvt_pk_bf16_f32 v3, v12, v13
	ds_write_b128 v105, v[0:3] offset:33808
	v_cvt_pk_bf16_f32 v0, v8, v9
	v_cvt_pk_bf16_f32 v1, v4, v5
	v_cvt_pk_bf16_f32 v2, v10, v11
	v_cvt_pk_bf16_f32 v3, v6, v7
	ds_write_b128 v105, v[0:3] offset:51216
	v_lshl_add_u64 v[0:1], v[16:17], 0, s[60:61]
	v_lshl_add_u64 v[0:1], v[0:1], 0, v[58:59]
	s_mov_b64 s[60:61], 0x1800
	v_lshl_add_u64 v[12:13], v[0:1], 0, s[60:61]
	v_add_co_u32_e32 v0, vcc, s28, v0
	s_nop 1
	v_addc_co_u32_e32 v1, vcc, 0, v1, vcc
	s_waitcnt vmcnt(0)
	ds_write_b128 v106, v[128:131]
	ds_write_b128 v107, v[156:159]
	ds_write_b128 v106, v[140:143] offset:16
	ds_write_b128 v107, v[152:155] offset:16
	ds_write_b128 v106, v[136:139] offset:32
	ds_write_b128 v107, v[148:151] offset:32
	ds_write_b128 v106, v[132:135] offset:48
	ds_write_b128 v107, v[144:147] offset:48
	v_add_co_u32_e32 v0, vcc, 0x8000, v28
	v_lshl_add_u64 v[12:13], v[28:29], 0, s[30:31]
	s_nop 0
	v_addc_co_u32_e32 v1, vcc, 0, v29, vcc
	global_load_dwordx4 v[8:11], v[0:1], off
	s_nop 0
	global_load_dwordx4 v[0:3], v[12:13], off offset:48
	global_load_dwordx4 v[4:7], v[12:13], off offset:32
	s_nop 0
	global_load_dwordx4 v[12:15], v[12:13], off offset:16
	s_waitcnt lgkmcnt(0)
	s_barrier
	v_mov_b32_e32 v16, 0
	s_andn2_b64 vcc, exec, s[40:41]
	v_mov_b32_e32 v17, 0
	v_mov_b32_e32 v18, 0
	v_mov_b32_e32 v19, 0
	v_mov_b32_e32 v20, 0
	s_cbranch_vccnz .LBB0_774
	ds_read_b128 v[18:21], v113 offset:51200
	ds_read_b128 v[22:25], v109 offset:33792
	s_waitcnt lgkmcnt(0)
	v_mfma_f32_16x16x32_bf16 v[18:21], v[18:21], v[22:25], 0
	ds_read_b128 v[22:25], v113 offset:51264
	ds_read_b128 v[26:29], v109 offset:33856
	s_waitcnt lgkmcnt(0)
	v_mfma_f32_16x16x32_bf16 v[18:21], v[22:25], v[26:29], v[18:21]
	ds_read_b128 v[22:25], v113 offset:51328
	ds_read_b128 v[26:29], v109 offset:33920
	s_waitcnt lgkmcnt(0)
	v_mfma_f32_16x16x32_bf16 v[18:21], v[22:25], v[26:29], v[18:21]
	ds_read_b128 v[22:25], v113 offset:51392
	ds_read_b128 v[26:29], v109 offset:33984
	s_waitcnt lgkmcnt(0)
	v_mfma_f32_16x16x32_bf16 v[18:21], v[22:25], v[26:29], v[18:21]
	v_mov_b32_e32 v22, s51
	s_nop 6
	v_cndmask_b32_e64 v17, v18, v22, s[10:11]
	v_cndmask_b32_e64 v17, v17, v18, s[12:13]
	v_cndmask_b32_e64 v18, 0, v19, s[12:13]
	v_cndmask_b32_e64 v19, v20, 0, s[14:15]
	v_cndmask_b32_e64 v20, v21, 0, s[16:17]
